# mLSTM Z unit: LDS reads of intra-chunk loop and inter-chunk block hoisted into unused registers with counted lgkmcnt waits
# baseline (speedup 1.0000x reference)
; #define LAS __attribute__((address_space(3)))
; __device__ __forceinline__ unsigned cvtpk(float lo, float hi) { f32x2 v = {lo, hi}; bf16x2_t b = __builtin_convertvector(v, bf16x2_t); return __builtin_bit_cast(unsigned, b); }
; __device__ __forceinline__ void z_unit(Frame& F, const bf16_t* proj, const float* gates, const MW& W, unsigned char* Y, int u, ZL& cur, ZL& nxt, bool has_next, int un) {
;     ...
;     for (int st = 0; st <= tt; ++st) {
;         f32x16 S;
; #pragma unroll
;         for (int r = 0; r < 16; ++r) S[r] = 0.f;
; #pragma unroll
;         for (int k = 0; k < 8; ++k) { const bf16x8 a = *(const LAS bf16x8*)(lds + KS + (32 * st + r32) * RS + (16 * k + 8 * hh) * 2); const bf16x8 qk = *(const LAS bf16x8*)(lds + QS + trow * RS + (16 * k + 8 * hh) * 2); S = __builtin_amdgcn_mfma_f32_32x32x16_bf16(a, qk, S, 0, 0, 0); }
;         const LAS float* csp = (const LAS float*)(lds + CSO) + 32 * st + 4 * hh;
; #pragma unroll
;         for (int r = 0; r < 16; ++r) { const int so = (r & 3) + 8 * (r >> 2); const float cv = csp[so];
;             const bool ok = (st < tt) || (so + 4 * hh <= r32);
;             const float p = ok ? S[r] * __expf(rt + cv) : 0.f; S[r] = p; den += p; }
; #pragma unroll
;         for (int k2 = 0; k2 < 2; ++k2) {
;             u32x4 pw; pw.x = cvtpk(S[8 * k2 + 0], S[8 * k2 + 1]); pw.y = cvtpk(S[8 * k2 + 2], S[8 * k2 + 3]); pw.z = cvtpk(S[8 * k2 + 4], S[8 * k2 + 5]); pw.w = cvtpk(S[8 * k2 + 6], S[8 * k2 + 7]);
;             const LAS unsigned char* vp = lds + VT + (32 * et + r32) * TS + (32 * st + 16 * k2 + 4 * hh) * 2;
;             const u32x2 lo = *(const LAS u32x2*)vp, hi = *(const LAS u32x2*)(vp + 16); u32x4 aw; aw.x = lo.x; aw.y = lo.y; aw.z = hi.x; aw.w = hi.y;
;             acc = __builtin_amdgcn_mfma_f32_32x32x16_bf16(__builtin_bit_cast(bf16x8, aw), __builtin_bit_cast(bf16x8, pw), acc, 0, 0, 0); }
;     }
.LBB0_682:
	v_add_u32_e32 v183, 0, v182
	ds_read_b128 v[210:213], v183
	ds_read_b128 v[214:217], v183 offset:32
	ds_read_b128 v[218:221], v183 offset:64
	ds_read_b128 v[222:225], v183 offset:96
	ds_read_b128 v[226:229], v183 offset:128
	ds_read_b128 v[230:233], v183 offset:160
	ds_read_b128 v[234:237], v183 offset:192
	ds_read_b128 v[238:241], v183 offset:224
	s_nop 0
	s_nop 0
	v_add_u32_e32 v188, 0, v110
	v_add_u32_e32 v209, 0x1ee00, v188
	ds_read_b128 v[242:245], v209
	ds_read_b128 v[246:249], v209 offset:32
	ds_read_b128 v[250:253], v209 offset:64
	s_cmp_lt_u32 s1, s3
	s_cselect_b64 s[46:47], -1, 0
	s_waitcnt lgkmcnt(11)
	s_waitcnt lgkmcnt(10)
	v_mfma_f32_32x32x16_bf16 v[18:33], v[210:213], v[78:81], 0
	ds_read_b128 v[210:213], v209 offset:96
	s_or_b64 vcc, s[10:11], s[46:47]
	s_add_i32 s1, s1, 1
	v_add_u32_e32 v182, 0x2200, v182
	v_add_u32_e32 v110, 0x80, v110
	s_nop 0
	s_waitcnt lgkmcnt(10)
	v_mfma_f32_32x32x16_bf16 v[18:33], v[214:217], v[82:85], v[18:33]
	s_nop 0
	s_nop 0
	s_waitcnt lgkmcnt(9)
	v_mfma_f32_32x32x16_bf16 v[18:33], v[218:221], v[86:89], v[18:33]
	s_nop 0
	s_nop 0
	s_waitcnt lgkmcnt(8)
	v_mfma_f32_32x32x16_bf16 v[18:33], v[222:225], v[90:93], v[18:33]
	s_nop 0
	s_nop 0
	s_waitcnt lgkmcnt(7)
	v_mfma_f32_32x32x16_bf16 v[18:33], v[226:229], v[94:97], v[18:33]
	s_nop 0
	s_nop 0
	s_waitcnt lgkmcnt(6)
	v_mfma_f32_32x32x16_bf16 v[18:33], v[230:233], v[98:101], v[18:33]
	s_nop 0
	s_nop 0
	s_waitcnt lgkmcnt(5)
	v_mfma_f32_32x32x16_bf16 v[18:33], v[234:237], v[102:105], v[18:33]
	s_nop 0
	s_nop 0
	s_nop 0
	s_waitcnt lgkmcnt(4)
	v_mfma_f32_32x32x16_bf16 v[18:33], v[238:241], v[106:109], v[18:33]
	s_nop 0
	s_nop 0
	s_waitcnt lgkmcnt(3)
	v_add_f32_e32 v183, v242, v181
	v_mul_f32_e32 v183, 0x3fb8aa3b, v183
	v_exp_f32_e32 v183, v183
	s_nop 6
	v_mul_f32_e32 v18, v18, v183
	v_cndmask_b32_e32 v183, 0, v18, vcc
	v_add_f32_e32 v18, v243, v181
	v_mul_f32_e32 v18, 0x3fb8aa3b, v18
	v_exp_f32_e32 v18, v18
	s_or_b64 vcc, s[46:47], s[12:13]
	v_add_f32_e32 v1, v1, v183
	v_mul_f32_e32 v18, v19, v18
	v_cndmask_b32_e32 v184, 0, v18, vcc
	v_add_f32_e32 v18, v244, v181
	v_mul_f32_e32 v18, 0x3fb8aa3b, v18
	v_exp_f32_e32 v18, v18
	s_or_b64 vcc, s[46:47], s[14:15]
	v_add_f32_e32 v1, v1, v184
	v_mul_f32_e32 v18, v20, v18
	v_cndmask_b32_e32 v185, 0, v18, vcc
	v_add_f32_e32 v18, v245, v181
	v_mul_f32_e32 v18, 0x3fb8aa3b, v18
	v_exp_f32_e32 v18, v18
	s_or_b64 vcc, s[46:47], s[16:17]
	v_add_f32_e32 v1, v1, v185
	v_mul_f32_e32 v18, v21, v18
	v_cndmask_b32_e32 v186, 0, v18, vcc
	s_nop 0
	s_nop 0
	s_or_b64 vcc, s[46:47], s[18:19]
	v_add_f32_e32 v1, v1, v186
	s_nop 0
	s_waitcnt lgkmcnt(2)
	v_add_f32_e32 v18, v246, v181
	v_mul_f32_e32 v18, 0x3fb8aa3b, v18
	v_exp_f32_e32 v18, v18
	s_nop 0
	v_mul_f32_e32 v18, v22, v18
	v_cndmask_b32_e32 v22, 0, v18, vcc
	v_add_f32_e32 v18, v247, v181
	v_mul_f32_e32 v18, 0x3fb8aa3b, v18
	v_exp_f32_e32 v18, v18
	s_or_b64 vcc, s[46:47], s[20:21]
	v_add_f32_e32 v1, v1, v22
	v_mul_f32_e32 v18, v23, v18
	v_cndmask_b32_e32 v23, 0, v18, vcc
	v_add_f32_e32 v18, v248, v181
	v_mul_f32_e32 v18, 0x3fb8aa3b, v18
	v_exp_f32_e32 v18, v18
	s_or_b64 vcc, s[46:47], s[22:23]
	v_add_f32_e32 v1, v1, v23
	v_mul_f32_e32 v18, v24, v18
	v_cndmask_b32_e32 v24, 0, v18, vcc
	v_add_f32_e32 v18, v249, v181
	v_mul_f32_e32 v18, 0x3fb8aa3b, v18
	v_exp_f32_e32 v18, v18
	s_or_b64 vcc, s[46:47], s[24:25]
	v_add_f32_e32 v1, v1, v24
	v_mul_f32_e32 v18, v25, v18
	v_cndmask_b32_e32 v25, 0, v18, vcc
	s_nop 0
	s_nop 0
	s_or_b64 vcc, s[46:47], s[26:27]
	v_add_f32_e32 v1, v1, v25
	s_nop 0
	s_waitcnt lgkmcnt(1)
	v_add_f32_e32 v18, v250, v181
	v_mul_f32_e32 v18, 0x3fb8aa3b, v18
	v_exp_f32_e32 v18, v18
	s_nop 0
	v_mul_f32_e32 v18, v26, v18
	v_cndmask_b32_e32 v187, 0, v18, vcc
	v_add_f32_e32 v18, v251, v181
	v_mul_f32_e32 v18, 0x3fb8aa3b, v18
	v_exp_f32_e32 v18, v18
	s_or_b64 vcc, s[46:47], s[28:29]
	v_add_f32_e32 v1, v1, v187
	v_mul_f32_e32 v18, v27, v18
	v_cndmask_b32_e32 v189, 0, v18, vcc
	v_add_f32_e32 v18, v252, v181
	v_mul_f32_e32 v18, 0x3fb8aa3b, v18
	v_exp_f32_e32 v18, v18
	s_or_b64 vcc, s[46:47], s[30:31]
	v_add_f32_e32 v1, v1, v189
	v_mul_f32_e32 v18, v28, v18
	v_cndmask_b32_e32 v190, 0, v18, vcc
	v_add_f32_e32 v18, v253, v181
	v_mul_f32_e32 v18, 0x3fb8aa3b, v18
	v_exp_f32_e32 v18, v18
	s_or_b64 vcc, s[46:47], s[34:35]
	v_add_f32_e32 v1, v1, v190
	v_mul_f32_e32 v18, v29, v18
	v_cndmask_b32_e32 v191, 0, v18, vcc
	s_nop 0
	s_nop 0
	v_add_u32_e32 v188, 0, v131
	v_add_u32_e32 v26, 0x11c00, v188
	ds_read_b64 v[26:27], v26
	s_or_b64 vcc, s[46:47], s[36:37]
	s_nop 0
	s_waitcnt lgkmcnt(1)
	v_add_f32_e32 v18, v210, v181
	v_mul_f32_e32 v18, 0x3fb8aa3b, v18
	v_exp_f32_e32 v18, v18
	v_add_u32_e32 v28, 0x11c10, v188
	ds_read_b64 v[28:29], v28
	v_add_f32_e32 v1, v1, v191
	v_mul_f32_e32 v18, v30, v18
	v_cndmask_b32_e32 v30, 0, v18, vcc
	v_add_f32_e32 v18, v211, v181
	v_mul_f32_e32 v18, 0x3fb8aa3b, v18
	v_exp_f32_e32 v18, v18
	s_or_b64 vcc, s[46:47], s[38:39]
	v_cvt_pk_bf16_f32 v19, v185, v186
	v_add_f32_e32 v1, v1, v30
	v_mul_f32_e32 v18, v31, v18
	v_cndmask_b32_e32 v31, 0, v18, vcc
	v_add_f32_e32 v18, v212, v181
	v_mul_f32_e32 v18, 0x3fb8aa3b, v18
	v_exp_f32_e32 v18, v18
	s_or_b64 vcc, s[46:47], s[40:41]
	v_cvt_pk_bf16_f32 v20, v22, v23
	v_add_f32_e32 v1, v1, v31
	v_mul_f32_e32 v18, v32, v18
	v_cndmask_b32_e32 v32, 0, v18, vcc
	v_add_f32_e32 v18, v213, v181
	v_mul_f32_e32 v18, 0x3fb8aa3b, v18
	v_exp_f32_e32 v18, v18
	s_or_b64 vcc, s[46:47], s[42:43]
	v_cvt_pk_bf16_f32 v21, v24, v25
	v_add_f32_e32 v1, v1, v32
	v_mul_f32_e32 v18, v33, v18
	v_cndmask_b32_e32 v33, 0, v18, vcc
	v_cvt_pk_bf16_f32 v18, v183, v184
	v_add_f32_e32 v1, v1, v33
	v_add_u32_e32 v131, 64, v131
	s_nop 0
	s_waitcnt lgkmcnt(0)
	v_mfma_f32_32x32x16_bf16 v[2:17], v[26:29], v[18:21], v[2:17]
	v_add_u32_e32 v26, 0x11c20, v188
	v_add_u32_e32 v28, 0x11c30, v188
	ds_read_b64 v[26:27], v26
	ds_read_b64 v[28:29], v28
	v_cvt_pk_bf16_f32 v18, v187, v189
	v_cvt_pk_bf16_f32 v19, v190, v191
	v_cvt_pk_bf16_f32 v20, v30, v31
	v_cvt_pk_bf16_f32 v21, v32, v33
	s_cmp_lg_u32 s49, s1
	s_nop 0
	s_waitcnt lgkmcnt(0)
	v_mfma_f32_32x32x16_bf16 v[2:17], v[26:29], v[18:21], v[2:17]
	s_cbranch_scc1 .LBB0_682
; #define LAS __attribute__((address_space(3)))
; __device__ __forceinline__ float bf1(bf16_t u) { return __uint_as_float(((unsigned)u) << 16); }
; __device__ __forceinline__ void z_unit(Frame& F, const bf16_t* proj, const float* gates, const MW& W, unsigned char* Y, int u, ZL& cur, ZL& nxt, bool has_next, int un) {
;     ...
;     {
;         const LAS float* nsp = (const LAS float*)(lds + NS);
; #pragma unroll
;         for (int k = 0; k < 8; ++k) {
;             const bf16x8 a = *(const LAS bf16x8*)(lds + CB + (32 * et + r32) * RS + (16 * k + 8 * hh) * 2);
;             const bf16x8 bq = *(const LAS bf16x8*)(lds + QW + trow * RS + (16 * k + 8 * hh) * 2);
;             acc = __builtin_amdgcn_mfma_f32_32x32x16_bf16(a, bq, acc, 0, 0, 0);
;             const f32x4 n0 = *(const LAS f32x4*)(nsp + 16 * k + 8 * hh), n1 = *(const LAS f32x4*)(nsp + 16 * k + 8 * hh + 4);
;             den += bf1((bf16_t)bq[0]) * n0[0] + bf1((bf16_t)bq[1]) * n0[1] + bf1((bf16_t)bq[2]) * n0[2] + bf1((bf16_t)bq[3]) * n0[3]
;                  + bf1((bf16_t)bq[4]) * n1[0] + bf1((bf16_t)bq[5]) * n1[1] + bf1((bf16_t)bq[6]) * n1[2] + bf1((bf16_t)bq[7]) * n1[3]; }
;     }
	ds_read_b128 v[210:213], v178 offset:17408
	ds_read_b128 v[214:217], v178 offset:17440
	ds_read_b128 v[218:221], v173
	ds_read_b128 v[222:225], v173 offset:32
	ds_read_b128 v[226:229], v174
	ds_read_b128 v[230:233], v174 offset:16
	ds_read_b128 v[234:237], v174 offset:64
	ds_read_b128 v[238:241], v174 offset:80
	ds_read_b128 v[242:245], v173 offset:64
	ds_read_b128 v[246:249], v178 offset:17472
	s_nop 0
	s_nop 0
	s_nop 0
	s_nop 0
	s_waitcnt lgkmcnt(10)
	s_waitcnt lgkmcnt(7)
	v_mfma_f32_32x32x16_bf16 v[2:17], v[218:221], v[210:213], v[2:17]
	ds_read_b128 v[250:253], v174 offset:128
	ds_read_b128 v[218:221], v174 offset:144
	s_nop 0
	s_nop 0
	v_lshlrev_b32_e32 v82, 16, v210
	v_and_b32_e32 v18, 0xffff0000, v210
	s_nop 0
	s_waitcnt lgkmcnt(7)
	v_mul_f32_e32 v18, v227, v18
	v_fmac_f32_e32 v18, v226, v82
	v_lshlrev_b32_e32 v26, 16, v211
	v_fmac_f32_e32 v18, v228, v26
	v_and_b32_e32 v19, 0xffff0000, v211
	v_fmac_f32_e32 v18, v229, v19
	ds_read_b128 v[226:229], v173 offset:96
	v_lshlrev_b32_e32 v19, 16, v212
	s_nop 0
	s_waitcnt lgkmcnt(7)
	v_fmac_f32_e32 v18, v230, v19
	v_and_b32_e32 v19, 0xffff0000, v212
	v_fmac_f32_e32 v18, v231, v19
	v_lshlrev_b32_e32 v19, 16, v213
	v_fmac_f32_e32 v18, v232, v19
	v_and_b32_e32 v19, 0xffff0000, v213
	ds_read_b128 v[210:213], v178 offset:17504
	v_fmac_f32_e32 v18, v233, v19
	v_add_f32_e32 v1, v1, v18
	s_nop 0
	s_nop 0
	v_mfma_f32_32x32x16_bf16 v[2:17], v[222:225], v[214:217], v[2:17]
	ds_read_b128 v[230:233], v174 offset:192
	ds_read_b128 v[222:225], v174 offset:208
	v_lshlrev_b32_e32 v30, 16, v214
	v_and_b32_e32 v22, 0xffff0000, v214
	s_nop 0
	s_waitcnt lgkmcnt(9)
	v_mul_f32_e32 v19, v235, v22
	v_fmac_f32_e32 v19, v234, v30
	v_lshlrev_b32_e32 v18, 16, v215
	v_fmac_f32_e32 v19, v236, v18
	v_and_b32_e32 v18, 0xffff0000, v215
	v_fmac_f32_e32 v19, v237, v18
	ds_read_b128 v[234:237], v173 offset:128
	v_lshlrev_b32_e32 v18, 16, v216
	s_nop 0
	s_waitcnt lgkmcnt(9)
	v_fmac_f32_e32 v19, v238, v18
	v_and_b32_e32 v18, 0xffff0000, v216
	v_fmac_f32_e32 v19, v239, v18
	v_lshlrev_b32_e32 v18, 16, v217
	v_fmac_f32_e32 v19, v240, v18
	v_and_b32_e32 v18, 0xffff0000, v217
	ds_read_b128 v[214:217], v178 offset:17536
	v_fmac_f32_e32 v19, v241, v18
	v_add_f32_e32 v1, v1, v19
	s_nop 0
	s_nop 0
	s_nop 0
	s_waitcnt lgkmcnt(8)
	v_mfma_f32_32x32x16_bf16 v[2:17], v[242:245], v[246:249], v[2:17]
	ds_read_b128 v[238:241], v174 offset:256
	ds_read_b128 v[242:245], v174 offset:272
	s_nop 0
	s_nop 0
	v_lshlrev_b32_e32 v30, 16, v246
	v_and_b32_e32 v22, 0xffff0000, v246
	s_nop 0
	s_waitcnt lgkmcnt(9)
	v_mul_f32_e32 v19, v251, v22
	v_fmac_f32_e32 v19, v250, v30
	v_lshlrev_b32_e32 v18, 16, v247
	v_fmac_f32_e32 v19, v252, v18
	v_and_b32_e32 v18, 0xffff0000, v247
	v_fmac_f32_e32 v19, v253, v18
	ds_read_b128 v[250:253], v173 offset:160
	v_lshlrev_b32_e32 v18, 16, v248
	s_nop 0
	s_waitcnt lgkmcnt(9)
	v_fmac_f32_e32 v19, v218, v18
	v_and_b32_e32 v18, 0xffff0000, v248
	v_fmac_f32_e32 v19, v219, v18
	v_lshlrev_b32_e32 v18, 16, v249
	v_fmac_f32_e32 v19, v220, v18
	v_and_b32_e32 v18, 0xffff0000, v249
	ds_read_b128 v[246:249], v178 offset:17568
	v_fmac_f32_e32 v19, v221, v18
	v_add_f32_e32 v1, v1, v19
	s_nop 0
	s_nop 0
	s_nop 0
	s_waitcnt lgkmcnt(8)
	v_mfma_f32_32x32x16_bf16 v[2:17], v[226:229], v[210:213], v[2:17]
	ds_read_b128 v[218:221], v174 offset:320
	ds_read_b128 v[226:229], v174 offset:336
	s_nop 0
	s_nop 0
	v_lshlrev_b32_e32 v30, 16, v210
	v_and_b32_e32 v22, 0xffff0000, v210
	s_nop 0
	s_waitcnt lgkmcnt(9)
	v_mul_f32_e32 v19, v231, v22
	v_fmac_f32_e32 v19, v230, v30
	v_lshlrev_b32_e32 v18, 16, v211
	v_fmac_f32_e32 v19, v232, v18
	v_and_b32_e32 v18, 0xffff0000, v211
	v_fmac_f32_e32 v19, v233, v18
	ds_read_b128 v[230:233], v173 offset:192
	v_lshlrev_b32_e32 v18, 16, v212
	s_nop 0
	s_waitcnt lgkmcnt(9)
	v_fmac_f32_e32 v19, v222, v18
	v_and_b32_e32 v18, 0xffff0000, v212
	v_fmac_f32_e32 v19, v223, v18
	v_lshlrev_b32_e32 v18, 16, v213
	v_fmac_f32_e32 v19, v224, v18
	v_and_b32_e32 v18, 0xffff0000, v213
	ds_read_b128 v[210:213], v178 offset:17600
	v_fmac_f32_e32 v19, v225, v18
	v_add_f32_e32 v1, v1, v19
	s_nop 0
	s_nop 0
	s_nop 0
	s_waitcnt lgkmcnt(8)
	v_mfma_f32_32x32x16_bf16 v[2:17], v[234:237], v[214:217], v[2:17]
	ds_read_b128 v[222:225], v174 offset:384
	ds_read_b128 v[234:237], v174 offset:400
	s_nop 0
	s_nop 0
	v_lshlrev_b32_e32 v30, 16, v214
	v_and_b32_e32 v22, 0xffff0000, v214
	s_nop 0
	s_waitcnt lgkmcnt(9)
; #define LAS __attribute__((address_space(3)))
; __device__ __forceinline__ float bf1(bf16_t u) { return __uint_as_float(((unsigned)u) << 16); }
; __device__ __forceinline__ void z_unit(Frame& F, const bf16_t* proj, const float* gates, const MW& W, unsigned char* Y, int u, ZL& cur, ZL& nxt, bool has_next, int un) {
;     ...
;     {
;         const LAS float* nsp = (const LAS float*)(lds + NS);
; #pragma unroll
;         for (int k = 0; k < 8; ++k) {
;             const bf16x8 a = *(const LAS bf16x8*)(lds + CB + (32 * et + r32) * RS + (16 * k + 8 * hh) * 2);
;             const bf16x8 bq = *(const LAS bf16x8*)(lds + QW + trow * RS + (16 * k + 8 * hh) * 2);
;             acc = __builtin_amdgcn_mfma_f32_32x32x16_bf16(a, bq, acc, 0, 0, 0);
;             const f32x4 n0 = *(const LAS f32x4*)(nsp + 16 * k + 8 * hh), n1 = *(const LAS f32x4*)(nsp + 16 * k + 8 * hh + 4);
;             den += bf1((bf16_t)bq[0]) * n0[0] + bf1((bf16_t)bq[1]) * n0[1] + bf1((bf16_t)bq[2]) * n0[2] + bf1((bf16_t)bq[3]) * n0[3]
;                  + bf1((bf16_t)bq[4]) * n1[0] + bf1((bf16_t)bq[5]) * n1[1] + bf1((bf16_t)bq[6]) * n1[2] + bf1((bf16_t)bq[7]) * n1[3]; }
;     }
;     den += __shfl_xor(den, 32);
;     const float hinv = 1.f / fmaxf(fabsf(den), eo);
;     float ssq = 0.f;
; #pragma unroll
;     for (int r = 0; r < 16; ++r) { acc[r] *= hinv; ssq += acc[r] * acc[r]; }
;     ssq += __shfl_xor(ssq, 32);
;     if (hh == 0) ((LAS float*)(lds + SSQ))[et * 64 + trow] = ssq;
	v_mul_f32_e32 v19, v239, v22
	v_fmac_f32_e32 v19, v238, v30
	v_lshlrev_b32_e32 v18, 16, v215
	v_fmac_f32_e32 v19, v240, v18
	v_and_b32_e32 v18, 0xffff0000, v215
	v_fmac_f32_e32 v19, v241, v18
	ds_read_b128 v[238:241], v173 offset:224
	v_lshlrev_b32_e32 v18, 16, v216
	s_nop 0
	s_waitcnt lgkmcnt(9)
	v_fmac_f32_e32 v19, v242, v18
	v_and_b32_e32 v18, 0xffff0000, v216
	v_fmac_f32_e32 v19, v243, v18
	v_lshlrev_b32_e32 v18, 16, v217
	v_fmac_f32_e32 v19, v244, v18
	v_and_b32_e32 v18, 0xffff0000, v217
	ds_read_b128 v[214:217], v178 offset:17632
	v_fmac_f32_e32 v19, v245, v18
	v_add_f32_e32 v1, v1, v19
	s_nop 0
	s_nop 0
	s_nop 0
	s_waitcnt lgkmcnt(8)
	v_mfma_f32_32x32x16_bf16 v[2:17], v[250:253], v[246:249], v[2:17]
	ds_read_b128 v[242:245], v174 offset:448
	ds_read_b128 v[250:253], v174 offset:464
	s_nop 0
	s_nop 0
	v_lshlrev_b32_e32 v30, 16, v246
	v_and_b32_e32 v22, 0xffff0000, v246
	s_nop 0
	s_waitcnt lgkmcnt(9)
	v_mul_f32_e32 v19, v219, v22
	v_fmac_f32_e32 v19, v218, v30
	v_lshlrev_b32_e32 v18, 16, v247
	v_fmac_f32_e32 v19, v220, v18
	v_and_b32_e32 v18, 0xffff0000, v247
	v_fmac_f32_e32 v19, v221, v18
	v_lshlrev_b32_e32 v18, 16, v248
	s_nop 0
	s_waitcnt lgkmcnt(8)
	v_fmac_f32_e32 v19, v226, v18
	v_and_b32_e32 v18, 0xffff0000, v248
	v_fmac_f32_e32 v19, v227, v18
	v_lshlrev_b32_e32 v18, 16, v249
	v_fmac_f32_e32 v19, v228, v18
	v_and_b32_e32 v18, 0xffff0000, v249
	v_fmac_f32_e32 v19, v229, v18
	v_add_f32_e32 v1, v1, v19
	s_nop 0
	s_nop 0
	s_nop 0
	s_waitcnt lgkmcnt(6)
	v_mfma_f32_32x32x16_bf16 v[2:17], v[230:233], v[210:213], v[2:17]
	s_nop 0
	s_nop 0
	v_lshlrev_b32_e32 v30, 16, v210
	v_and_b32_e32 v22, 0xffff0000, v210
	s_nop 0
	s_waitcnt lgkmcnt(5)
	v_mul_f32_e32 v19, v223, v22
	v_fmac_f32_e32 v19, v222, v30
	v_lshlrev_b32_e32 v18, 16, v211
	v_fmac_f32_e32 v19, v224, v18
	v_and_b32_e32 v18, 0xffff0000, v211
	v_fmac_f32_e32 v19, v225, v18
	v_lshlrev_b32_e32 v18, 16, v212
	s_nop 0
	s_waitcnt lgkmcnt(4)
	v_fmac_f32_e32 v19, v234, v18
	v_and_b32_e32 v18, 0xffff0000, v212
	v_fmac_f32_e32 v19, v235, v18
	v_lshlrev_b32_e32 v18, 16, v213
	v_fmac_f32_e32 v19, v236, v18
	v_and_b32_e32 v18, 0xffff0000, v213
	v_fmac_f32_e32 v19, v237, v18
	v_add_f32_e32 v1, v1, v19
	s_nop 0
	s_nop 0
	s_nop 0
	s_waitcnt lgkmcnt(2)
	v_mfma_f32_32x32x16_bf16 v[2:17], v[238:241], v[214:217], v[2:17]
	s_nop 0
	s_nop 0
	v_lshlrev_b32_e32 v30, 16, v214
	v_and_b32_e32 v22, 0xffff0000, v214
	s_nop 0
	s_waitcnt lgkmcnt(1)
	v_mul_f32_e32 v19, v243, v22
	v_fmac_f32_e32 v19, v242, v30
	v_lshlrev_b32_e32 v18, 16, v215
	v_fmac_f32_e32 v19, v244, v18
	v_and_b32_e32 v18, 0xffff0000, v215
	v_fmac_f32_e32 v19, v245, v18
	v_lshlrev_b32_e32 v18, 16, v216
	s_nop 0
	s_waitcnt lgkmcnt(0)
	v_fmac_f32_e32 v19, v250, v18
	v_and_b32_e32 v18, 0xffff0000, v216
	v_fmac_f32_e32 v19, v251, v18
	v_lshlrev_b32_e32 v18, 16, v217
	v_fmac_f32_e32 v19, v252, v18
	v_and_b32_e32 v18, 0xffff0000, v217
	v_fmac_f32_e32 v19, v253, v18
	v_add_f32_e32 v1, v1, v19
	ds_bpermute_b32 v18, v146, v1
	s_waitcnt lgkmcnt(0)
	v_add_f32_e32 v1, v1, v18
	v_max_f32_e32 v18, v180, v180
	v_max_f32_e64 v1, |v1|, v18
	v_div_scale_f32 v18, s[46:47], v1, v1, 1.0
	v_rcp_f32_e32 v19, v18
	s_nop 0
	v_fma_f32 v20, -v18, v19, 1.0
	v_fmac_f32_e32 v19, v20, v19
	v_div_scale_f32 v20, vcc, 1.0, v1, 1.0
	v_mul_f32_e32 v21, v20, v19
	v_fma_f32 v22, -v18, v21, v20
	v_fmac_f32_e32 v21, v22, v19
	v_fma_f32 v18, -v18, v21, v20
	v_div_fmas_f32 v18, v18, v19, v21
	v_div_fixup_f32 v1, v18, v1, 1.0
	v_mul_f32_e32 v25, v3, v1
	v_mul_f32_e32 v26, v2, v1
	v_mul_f32_e32 v2, v25, v25
	v_fmac_f32_e32 v2, v26, v26
	v_mul_f32_e32 v24, v4, v1
	v_fmac_f32_e32 v2, v24, v24
	v_mul_f32_e32 v23, v5, v1
	v_fmac_f32_e32 v2, v23, v23
	v_mul_f32_e32 v22, v6, v1
	v_fmac_f32_e32 v2, v22, v22
	v_mul_f32_e32 v21, v7, v1
	v_fmac_f32_e32 v2, v21, v21
	v_mul_f32_e32 v20, v8, v1
	v_fmac_f32_e32 v2, v20, v20
	v_mul_f32_e32 v19, v9, v1
	v_fmac_f32_e32 v2, v19, v19
	v_mul_f32_e32 v18, v10, v1
	v_fmac_f32_e32 v2, v18, v18
	v_mul_f32_e32 v10, v11, v1
	v_fmac_f32_e32 v2, v10, v10
	v_mul_f32_e32 v9, v12, v1
	v_fmac_f32_e32 v2, v9, v9
	v_mul_f32_e32 v8, v13, v1
	v_fmac_f32_e32 v2, v8, v8
	v_mul_f32_e32 v6, v14, v1
	v_fmac_f32_e32 v2, v6, v6
	v_mul_f32_e32 v5, v15, v1
	v_fmac_f32_e32 v2, v5, v5
	v_mul_f32_e32 v4, v16, v1
	v_fmac_f32_e32 v2, v4, v4
	v_mul_f32_e32 v1, v17, v1
	v_fmac_f32_e32 v2, v1, v1
	ds_bpermute_b32 v3, v146, v2
	s_and_saveexec_b64 s[46:47], s[44:45]
	s_cbranch_execz .LBB0_658
	s_waitcnt lgkmcnt(0)
	v_add_f32_e32 v2, v2, v3
	v_add_u32_e32 v3, s4, v149
	ds_write_b32 v3, v2
	s_branch .LBB0_658

; #define LAS __attribute__((address_space(3)))
; __device__ __forceinline__ unsigned cvtpk(float lo, float hi) { f32x2 v = {lo, hi}; bf16x2_t b = __builtin_convertvector(v, bf16x2_t); return __builtin_bit_cast(unsigned, b); }
; __device__ __forceinline__ void z_unit(Frame& F, const bf16_t* proj, const float* gates, const MW& W, unsigned char* Y, int u, ZL& cur, ZL& nxt, bool has_next, int un) {
;     ...
;     for (int st = 0; st <= tt; ++st) {
;         f32x16 S;
; #pragma unroll
;         for (int r = 0; r < 16; ++r) S[r] = 0.f;
; #pragma unroll
;         for (int k = 0; k < 8; ++k) { const bf16x8 a = *(const LAS bf16x8*)(lds + KS + (32 * st + r32) * RS + (16 * k + 8 * hh) * 2); const bf16x8 qk = *(const LAS bf16x8*)(lds + QS + trow * RS + (16 * k + 8 * hh) * 2); S = __builtin_amdgcn_mfma_f32_32x32x16_bf16(a, qk, S, 0, 0, 0); }
;         const LAS float* csp = (const LAS float*)(lds + CSO) + 32 * st + 4 * hh;
; #pragma unroll
;         for (int r = 0; r < 16; ++r) { const int so = (r & 3) + 8 * (r >> 2); const float cv = csp[so];
;             const bool ok = (st < tt) || (so + 4 * hh <= r32);
;             const float p = ok ? S[r] * __expf(rt + cv) : 0.f; S[r] = p; den += p; }
; #pragma unroll
;         for (int k2 = 0; k2 < 2; ++k2) {
;             u32x4 pw; pw.x = cvtpk(S[8 * k2 + 0], S[8 * k2 + 1]); pw.y = cvtpk(S[8 * k2 + 2], S[8 * k2 + 3]); pw.z = cvtpk(S[8 * k2 + 4], S[8 * k2 + 5]); pw.w = cvtpk(S[8 * k2 + 6], S[8 * k2 + 7]);
;             const LAS unsigned char* vp = lds + VT + (32 * et + r32) * TS + (32 * st + 16 * k2 + 4 * hh) * 2;
;             const u32x2 lo = *(const LAS u32x2*)vp, hi = *(const LAS u32x2*)(vp + 16); u32x4 aw; aw.x = lo.x; aw.y = lo.y; aw.z = hi.x; aw.w = hi.y;
;             acc = __builtin_amdgcn_mfma_f32_32x32x16_bf16(__builtin_bit_cast(bf16x8, aw), __builtin_bit_cast(bf16x8, pw), acc, 0, 0, 0); }
;     }
.LBB0_1810:
	v_add_u32_e32 v183, 0, v182
	ds_read_b128 v[210:213], v183
	ds_read_b128 v[214:217], v183 offset:32
	ds_read_b128 v[218:221], v183 offset:64
	ds_read_b128 v[222:225], v183 offset:96
	ds_read_b128 v[226:229], v183 offset:128
	ds_read_b128 v[230:233], v183 offset:160
	ds_read_b128 v[234:237], v183 offset:192
	ds_read_b128 v[238:241], v183 offset:224
	s_nop 0
	s_nop 0
	v_add_u32_e32 v188, 0, v131
	v_add_u32_e32 v209, 0x1ee00, v188
	ds_read_b128 v[242:245], v209
	ds_read_b128 v[246:249], v209 offset:32
	ds_read_b128 v[250:253], v209 offset:64
	s_cmp_lt_u32 s1, s3
	s_cselect_b64 s[46:47], -1, 0
	s_waitcnt lgkmcnt(11)
	s_waitcnt lgkmcnt(10)
	v_mfma_f32_32x32x16_bf16 v[18:33], v[210:213], v[78:81], 0
	ds_read_b128 v[210:213], v209 offset:96
	s_or_b64 vcc, s[10:11], s[46:47]
	s_add_i32 s1, s1, 1
	v_add_u32_e32 v182, 0x2200, v182
	v_add_u32_e32 v131, 0x80, v131
	s_nop 0
	s_waitcnt lgkmcnt(10)
	v_mfma_f32_32x32x16_bf16 v[18:33], v[214:217], v[82:85], v[18:33]
	s_nop 0
	s_nop 0
	s_waitcnt lgkmcnt(9)
	v_mfma_f32_32x32x16_bf16 v[18:33], v[218:221], v[86:89], v[18:33]
	s_nop 0
	s_nop 0
	s_waitcnt lgkmcnt(8)
	v_mfma_f32_32x32x16_bf16 v[18:33], v[222:225], v[90:93], v[18:33]
	s_nop 0
	s_nop 0
	s_waitcnt lgkmcnt(7)
	v_mfma_f32_32x32x16_bf16 v[18:33], v[226:229], v[94:97], v[18:33]
	s_nop 0
	s_nop 0
	s_waitcnt lgkmcnt(6)
	v_mfma_f32_32x32x16_bf16 v[18:33], v[230:233], v[98:101], v[18:33]
	s_nop 0
	s_nop 0
	s_waitcnt lgkmcnt(5)
	v_mfma_f32_32x32x16_bf16 v[18:33], v[234:237], v[102:105], v[18:33]
	s_nop 0
	s_nop 0
	s_nop 0
	s_waitcnt lgkmcnt(4)
	v_mfma_f32_32x32x16_bf16 v[18:33], v[238:241], v[106:109], v[18:33]
	s_nop 0
	s_nop 0
	s_waitcnt lgkmcnt(3)
	v_add_f32_e32 v183, v242, v180
	v_mul_f32_e32 v183, 0x3fb8aa3b, v183
	v_exp_f32_e32 v183, v183
	s_nop 6
	v_mul_f32_e32 v18, v18, v183
	v_cndmask_b32_e32 v183, 0, v18, vcc
	v_add_f32_e32 v18, v243, v180
	v_mul_f32_e32 v18, 0x3fb8aa3b, v18
	v_exp_f32_e32 v18, v18
	s_or_b64 vcc, s[46:47], s[12:13]
	v_mul_f32_e32 v18, v19, v18
	v_cndmask_b32_e32 v184, 0, v18, vcc
	v_add_f32_e32 v18, v244, v180
	v_mul_f32_e32 v18, 0x3fb8aa3b, v18
	v_exp_f32_e32 v18, v18
	s_or_b64 vcc, s[46:47], s[14:15]
	v_mul_f32_e32 v18, v20, v18
	v_cndmask_b32_e32 v185, 0, v18, vcc
	v_add_f32_e32 v18, v245, v180
	v_mul_f32_e32 v18, 0x3fb8aa3b, v18
	v_exp_f32_e32 v18, v18
	s_or_b64 vcc, s[46:47], s[16:17]
	v_mul_f32_e32 v18, v21, v18
	v_cndmask_b32_e32 v186, 0, v18, vcc
	s_nop 0
	s_nop 0
	s_or_b64 vcc, s[46:47], s[18:19]
	s_nop 0
	s_waitcnt lgkmcnt(2)
	v_add_f32_e32 v18, v246, v180
	v_mul_f32_e32 v18, 0x3fb8aa3b, v18
	v_exp_f32_e32 v18, v18
	s_nop 0
	v_mul_f32_e32 v18, v22, v18
	v_cndmask_b32_e32 v22, 0, v18, vcc
	v_add_f32_e32 v18, v247, v180
	v_mul_f32_e32 v18, 0x3fb8aa3b, v18
	v_exp_f32_e32 v18, v18
	s_or_b64 vcc, s[46:47], s[20:21]
	v_mul_f32_e32 v18, v23, v18
	v_cndmask_b32_e32 v23, 0, v18, vcc
	v_add_f32_e32 v18, v248, v180
	v_mul_f32_e32 v18, 0x3fb8aa3b, v18
	v_exp_f32_e32 v18, v18
	s_or_b64 vcc, s[46:47], s[22:23]
	v_mul_f32_e32 v18, v24, v18
	v_cndmask_b32_e32 v24, 0, v18, vcc
	v_add_f32_e32 v18, v249, v180
	v_mul_f32_e32 v18, 0x3fb8aa3b, v18
	v_exp_f32_e32 v18, v18
	s_or_b64 vcc, s[46:47], s[24:25]
	v_mul_f32_e32 v18, v25, v18
	v_cndmask_b32_e32 v25, 0, v18, vcc
	s_nop 0
	s_nop 0
	s_or_b64 vcc, s[46:47], s[26:27]
	s_nop 0
	s_waitcnt lgkmcnt(1)
	v_add_f32_e32 v18, v250, v180
	v_mul_f32_e32 v18, 0x3fb8aa3b, v18
	v_exp_f32_e32 v18, v18
	s_nop 0
	v_mul_f32_e32 v18, v26, v18
	v_cndmask_b32_e32 v187, 0, v18, vcc
	v_add_f32_e32 v18, v251, v180
	v_mul_f32_e32 v18, 0x3fb8aa3b, v18
	v_exp_f32_e32 v18, v18
	s_or_b64 vcc, s[46:47], s[28:29]
	v_mul_f32_e32 v18, v27, v18
	v_cndmask_b32_e32 v189, 0, v18, vcc
	v_add_f32_e32 v18, v252, v180
	v_mul_f32_e32 v18, 0x3fb8aa3b, v18
	v_exp_f32_e32 v18, v18
	s_or_b64 vcc, s[46:47], s[30:31]
	v_mul_f32_e32 v18, v28, v18
	v_cndmask_b32_e32 v190, 0, v18, vcc
	v_add_f32_e32 v18, v253, v180
	v_mul_f32_e32 v18, 0x3fb8aa3b, v18
	v_exp_f32_e32 v18, v18
	s_or_b64 vcc, s[46:47], s[34:35]
	v_mul_f32_e32 v18, v29, v18
	v_cndmask_b32_e32 v191, 0, v18, vcc
	s_nop 0
	s_nop 0
	v_add_u32_e32 v188, 0, v181
	v_add_u32_e32 v26, 0x11c00, v188
	ds_read_b64 v[26:27], v26
	s_or_b64 vcc, s[46:47], s[36:37]
	s_nop 0
	s_waitcnt lgkmcnt(1)
	v_add_f32_e32 v18, v210, v180
	v_mul_f32_e32 v18, 0x3fb8aa3b, v18
	v_exp_f32_e32 v18, v18
	v_add_u32_e32 v28, 0x11c10, v188
	ds_read_b64 v[28:29], v28
	v_add_u32_e32 v181, 64, v181
	v_mul_f32_e32 v18, v30, v18
	v_cndmask_b32_e32 v30, 0, v18, vcc
	v_add_f32_e32 v18, v211, v180
	v_mul_f32_e32 v18, 0x3fb8aa3b, v18
	v_exp_f32_e32 v18, v18
	s_or_b64 vcc, s[46:47], s[38:39]
	v_cvt_pk_bf16_f32 v19, v185, v186
	v_mul_f32_e32 v18, v31, v18
	v_cndmask_b32_e32 v31, 0, v18, vcc
	v_add_f32_e32 v18, v212, v180
	v_mul_f32_e32 v18, 0x3fb8aa3b, v18
	v_exp_f32_e32 v18, v18
	s_or_b64 vcc, s[46:47], s[40:41]
	v_cvt_pk_bf16_f32 v20, v22, v23
	v_mul_f32_e32 v18, v32, v18
	v_cndmask_b32_e32 v32, 0, v18, vcc
	v_add_f32_e32 v18, v213, v180
	v_mul_f32_e32 v18, 0x3fb8aa3b, v18
	v_exp_f32_e32 v18, v18
	s_or_b64 vcc, s[46:47], s[42:43]
	v_cvt_pk_bf16_f32 v21, v24, v25
	s_cmp_lg_u32 s49, s1
	v_mul_f32_e32 v18, v33, v18
	v_cndmask_b32_e32 v33, 0, v18, vcc
	v_cvt_pk_bf16_f32 v18, v183, v184
	s_nop 0
	s_nop 0
	s_waitcnt lgkmcnt(0)
	v_mfma_f32_32x32x16_bf16 v[2:17], v[26:29], v[18:21], v[2:17]
	v_add_u32_e32 v26, 0x11c20, v188
	v_add_u32_e32 v28, 0x11c30, v188
	ds_read_b64 v[26:27], v26
	ds_read_b64 v[28:29], v28
	v_cvt_pk_bf16_f32 v18, v187, v189
	v_cvt_pk_bf16_f32 v19, v190, v191
	v_cvt_pk_bf16_f32 v20, v30, v31
	v_cvt_pk_bf16_f32 v21, v32, v33
	s_nop 0
	s_nop 0
	s_waitcnt lgkmcnt(0)
	v_mfma_f32_32x32x16_bf16 v[2:17], v[26:29], v[18:21], v[2:17]
	v_add_f32_e32 v18, v110, v183
	v_add_f32_e32 v18, v18, v184
	v_add_f32_e32 v18, v18, v185
	v_add_f32_e32 v18, v18, v186
	v_add_f32_e32 v18, v18, v22
	v_add_f32_e32 v18, v18, v23
	v_add_f32_e32 v18, v18, v24
	v_add_f32_e32 v18, v18, v25
	v_add_f32_e32 v18, v18, v187
	v_add_f32_e32 v18, v18, v189
	v_add_f32_e32 v18, v18, v190
	v_add_f32_e32 v18, v18, v191
	v_add_f32_e32 v18, v18, v30
	v_add_f32_e32 v18, v18, v31
	v_add_f32_e32 v18, v18, v32
	v_add_f32_e32 v110, v18, v33
	s_cbranch_scc1 .LBB0_1810
; #define LAS __attribute__((address_space(3)))
; __device__ __forceinline__ float bf1(bf16_t u) { return __uint_as_float(((unsigned)u) << 16); }
; __device__ __forceinline__ void z_unit(Frame& F, const bf16_t* proj, const float* gates, const MW& W, unsigned char* Y, int u, ZL& cur, ZL& nxt, bool has_next, int un) {
;     ...
;     {
;         const LAS float* nsp = (const LAS float*)(lds + NS);
; #pragma unroll
;         for (int k = 0; k < 8; ++k) {
;             const bf16x8 a = *(const LAS bf16x8*)(lds + CB + (32 * et + r32) * RS + (16 * k + 8 * hh) * 2);
;             const bf16x8 bq = *(const LAS bf16x8*)(lds + QW + trow * RS + (16 * k + 8 * hh) * 2);
;             acc = __builtin_amdgcn_mfma_f32_32x32x16_bf16(a, bq, acc, 0, 0, 0);
;             const f32x4 n0 = *(const LAS f32x4*)(nsp + 16 * k + 8 * hh), n1 = *(const LAS f32x4*)(nsp + 16 * k + 8 * hh + 4);
;             den += bf1((bf16_t)bq[0]) * n0[0] + bf1((bf16_t)bq[1]) * n0[1] + bf1((bf16_t)bq[2]) * n0[2] + bf1((bf16_t)bq[3]) * n0[3]
;                  + bf1((bf16_t)bq[4]) * n1[0] + bf1((bf16_t)bq[5]) * n1[1] + bf1((bf16_t)bq[6]) * n1[2] + bf1((bf16_t)bq[7]) * n1[3]; }
;     }
	ds_read_b128 v[210:213], v177 offset:17408
	ds_read_b128 v[214:217], v177 offset:17440
	ds_read_b128 v[218:221], v172
	ds_read_b128 v[222:225], v172 offset:32
	ds_read_b128 v[226:229], v173
	ds_read_b128 v[230:233], v173 offset:16
	ds_read_b128 v[234:237], v173 offset:64
	ds_read_b128 v[238:241], v173 offset:80
	ds_read_b128 v[242:245], v172 offset:64
	ds_read_b128 v[246:249], v177 offset:17472
	s_nop 0
	s_nop 0
	s_nop 0
	s_nop 0
	s_waitcnt lgkmcnt(10)
	s_waitcnt lgkmcnt(7)
	v_mfma_f32_32x32x16_bf16 v[2:17], v[218:221], v[210:213], v[2:17]
	ds_read_b128 v[250:253], v173 offset:128
	ds_read_b128 v[218:221], v173 offset:144
	s_nop 0
	s_nop 0
	v_lshlrev_b32_e32 v82, 16, v210
	v_and_b32_e32 v18, 0xffff0000, v210
	s_nop 0
	s_waitcnt lgkmcnt(7)
	v_mul_f32_e32 v18, v227, v18
	v_fmac_f32_e32 v18, v226, v82
	v_lshlrev_b32_e32 v26, 16, v211
	v_fmac_f32_e32 v18, v228, v26
	v_and_b32_e32 v19, 0xffff0000, v211
	v_fmac_f32_e32 v18, v229, v19
	ds_read_b128 v[226:229], v172 offset:96
	v_lshlrev_b32_e32 v19, 16, v212
	s_nop 0
	s_waitcnt lgkmcnt(7)
	v_fmac_f32_e32 v18, v230, v19
	v_and_b32_e32 v19, 0xffff0000, v212
	v_fmac_f32_e32 v18, v231, v19
	v_lshlrev_b32_e32 v19, 16, v213
	v_fmac_f32_e32 v18, v232, v19
	v_and_b32_e32 v19, 0xffff0000, v213
	ds_read_b128 v[210:213], v177 offset:17504
	v_fmac_f32_e32 v18, v233, v19
	v_add_f32_e32 v78, v110, v18
	s_nop 0
	s_nop 0
	v_mfma_f32_32x32x16_bf16 v[2:17], v[222:225], v[214:217], v[2:17]
	ds_read_b128 v[230:233], v173 offset:192
	ds_read_b128 v[222:225], v173 offset:208
	v_lshlrev_b32_e32 v30, 16, v214
	v_and_b32_e32 v22, 0xffff0000, v214
	s_nop 0
	s_waitcnt lgkmcnt(9)
	v_mul_f32_e32 v19, v235, v22
	v_fmac_f32_e32 v19, v234, v30
	v_lshlrev_b32_e32 v18, 16, v215
	v_fmac_f32_e32 v19, v236, v18
	v_and_b32_e32 v18, 0xffff0000, v215
	v_fmac_f32_e32 v19, v237, v18
	ds_read_b128 v[234:237], v172 offset:128
	v_lshlrev_b32_e32 v18, 16, v216
	s_nop 0
	s_waitcnt lgkmcnt(9)
	v_fmac_f32_e32 v19, v238, v18
	v_and_b32_e32 v18, 0xffff0000, v216
	v_fmac_f32_e32 v19, v239, v18
	v_lshlrev_b32_e32 v18, 16, v217
	v_fmac_f32_e32 v19, v240, v18
	v_and_b32_e32 v18, 0xffff0000, v217
	ds_read_b128 v[214:217], v177 offset:17536
	v_fmac_f32_e32 v19, v241, v18
	v_add_f32_e32 v30, v78, v19
	s_nop 0
	s_nop 0
	s_nop 0
	s_waitcnt lgkmcnt(8)
	v_mfma_f32_32x32x16_bf16 v[2:17], v[242:245], v[246:249], v[2:17]
	ds_read_b128 v[238:241], v173 offset:256
	ds_read_b128 v[242:245], v173 offset:272
	s_nop 0
	s_nop 0
	v_lshlrev_b32_e32 v31, 16, v246
	v_and_b32_e32 v22, 0xffff0000, v246
	s_nop 0
	s_waitcnt lgkmcnt(9)
	v_mul_f32_e32 v19, v251, v22
	v_fmac_f32_e32 v19, v250, v31
	v_lshlrev_b32_e32 v18, 16, v247
	v_fmac_f32_e32 v19, v252, v18
	v_and_b32_e32 v18, 0xffff0000, v247
	v_fmac_f32_e32 v19, v253, v18
	ds_read_b128 v[250:253], v172 offset:160
	v_lshlrev_b32_e32 v18, 16, v248
	s_nop 0
	s_waitcnt lgkmcnt(9)
	v_fmac_f32_e32 v19, v218, v18
	v_and_b32_e32 v18, 0xffff0000, v248
	v_fmac_f32_e32 v19, v219, v18
	v_lshlrev_b32_e32 v18, 16, v249
	v_fmac_f32_e32 v19, v220, v18
	v_and_b32_e32 v18, 0xffff0000, v249
	ds_read_b128 v[246:249], v177 offset:17568
	v_fmac_f32_e32 v19, v221, v18
	v_add_f32_e32 v30, v30, v19
	s_nop 0
	s_nop 0
	s_nop 0
	s_waitcnt lgkmcnt(8)
	v_mfma_f32_32x32x16_bf16 v[2:17], v[226:229], v[210:213], v[2:17]
	ds_read_b128 v[218:221], v173 offset:320
	ds_read_b128 v[226:229], v173 offset:336
	s_nop 0
	s_nop 0
	v_lshlrev_b32_e32 v31, 16, v210
	v_and_b32_e32 v22, 0xffff0000, v210
	s_nop 0
	s_waitcnt lgkmcnt(9)
	v_mul_f32_e32 v19, v231, v22
	v_fmac_f32_e32 v19, v230, v31
	v_lshlrev_b32_e32 v18, 16, v211
	v_fmac_f32_e32 v19, v232, v18
	v_and_b32_e32 v18, 0xffff0000, v211
	v_fmac_f32_e32 v19, v233, v18
	ds_read_b128 v[230:233], v172 offset:192
	v_lshlrev_b32_e32 v18, 16, v212
	s_nop 0
	s_waitcnt lgkmcnt(9)
	v_fmac_f32_e32 v19, v222, v18
	v_and_b32_e32 v18, 0xffff0000, v212
	v_fmac_f32_e32 v19, v223, v18
	v_lshlrev_b32_e32 v18, 16, v213
	v_fmac_f32_e32 v19, v224, v18
	v_and_b32_e32 v18, 0xffff0000, v213
	ds_read_b128 v[210:213], v177 offset:17600
	v_fmac_f32_e32 v19, v225, v18
	v_add_f32_e32 v30, v30, v19
	s_nop 0
	s_nop 0
	s_nop 0
	s_waitcnt lgkmcnt(8)
	v_mfma_f32_32x32x16_bf16 v[2:17], v[234:237], v[214:217], v[2:17]
	ds_read_b128 v[222:225], v173 offset:384
	ds_read_b128 v[234:237], v173 offset:400
	s_nop 0
	s_nop 0
	v_lshlrev_b32_e32 v31, 16, v214
	v_and_b32_e32 v22, 0xffff0000, v214
	s_nop 0
	s_waitcnt lgkmcnt(9)
; #define LAS __attribute__((address_space(3)))
; __device__ __forceinline__ float bf1(bf16_t u) { return __uint_as_float(((unsigned)u) << 16); }
; __device__ __forceinline__ void z_unit(Frame& F, const bf16_t* proj, const float* gates, const MW& W, unsigned char* Y, int u, ZL& cur, ZL& nxt, bool has_next, int un) {
;     ...
;     {
;         const LAS float* nsp = (const LAS float*)(lds + NS);
; #pragma unroll
;         for (int k = 0; k < 8; ++k) {
;             const bf16x8 a = *(const LAS bf16x8*)(lds + CB + (32 * et + r32) * RS + (16 * k + 8 * hh) * 2);
;             const bf16x8 bq = *(const LAS bf16x8*)(lds + QW + trow * RS + (16 * k + 8 * hh) * 2);
;             acc = __builtin_amdgcn_mfma_f32_32x32x16_bf16(a, bq, acc, 0, 0, 0);
;             const f32x4 n0 = *(const LAS f32x4*)(nsp + 16 * k + 8 * hh), n1 = *(const LAS f32x4*)(nsp + 16 * k + 8 * hh + 4);
;             den += bf1((bf16_t)bq[0]) * n0[0] + bf1((bf16_t)bq[1]) * n0[1] + bf1((bf16_t)bq[2]) * n0[2] + bf1((bf16_t)bq[3]) * n0[3]
;                  + bf1((bf16_t)bq[4]) * n1[0] + bf1((bf16_t)bq[5]) * n1[1] + bf1((bf16_t)bq[6]) * n1[2] + bf1((bf16_t)bq[7]) * n1[3]; }
;     }
;     den += __shfl_xor(den, 32);
;     const float hinv = 1.f / fmaxf(fabsf(den), eo);
;     float ssq = 0.f;
; #pragma unroll
;     for (int r = 0; r < 16; ++r) { acc[r] *= hinv; ssq += acc[r] * acc[r]; }
;     ssq += __shfl_xor(ssq, 32);
;     if (hh == 0) ((LAS float*)(lds + SSQ))[et * 64 + trow] = ssq;
	v_mul_f32_e32 v19, v239, v22
	v_fmac_f32_e32 v19, v238, v31
	v_lshlrev_b32_e32 v18, 16, v215
	v_fmac_f32_e32 v19, v240, v18
	v_and_b32_e32 v18, 0xffff0000, v215
	v_fmac_f32_e32 v19, v241, v18
	ds_read_b128 v[238:241], v172 offset:224
	v_lshlrev_b32_e32 v18, 16, v216
	s_nop 0
	s_waitcnt lgkmcnt(9)
	v_fmac_f32_e32 v19, v242, v18
	v_and_b32_e32 v18, 0xffff0000, v216
	v_fmac_f32_e32 v19, v243, v18
	v_lshlrev_b32_e32 v18, 16, v217
	v_fmac_f32_e32 v19, v244, v18
	v_and_b32_e32 v18, 0xffff0000, v217
	ds_read_b128 v[214:217], v177 offset:17632
	v_fmac_f32_e32 v19, v245, v18
	v_add_f32_e32 v30, v30, v19
	s_nop 0
	s_nop 0
	s_nop 0
	s_waitcnt lgkmcnt(8)
	v_mfma_f32_32x32x16_bf16 v[2:17], v[250:253], v[246:249], v[2:17]
	ds_read_b128 v[242:245], v173 offset:448
	ds_read_b128 v[250:253], v173 offset:464
	s_nop 0
	s_nop 0
	v_lshlrev_b32_e32 v31, 16, v246
	v_and_b32_e32 v22, 0xffff0000, v246
	s_nop 0
	s_waitcnt lgkmcnt(9)
	v_mul_f32_e32 v19, v219, v22
	v_fmac_f32_e32 v19, v218, v31
	v_lshlrev_b32_e32 v18, 16, v247
	v_fmac_f32_e32 v19, v220, v18
	v_and_b32_e32 v18, 0xffff0000, v247
	v_fmac_f32_e32 v19, v221, v18
	v_lshlrev_b32_e32 v18, 16, v248
	s_nop 0
	s_waitcnt lgkmcnt(8)
	v_fmac_f32_e32 v19, v226, v18
	v_and_b32_e32 v18, 0xffff0000, v248
	v_fmac_f32_e32 v19, v227, v18
	v_lshlrev_b32_e32 v18, 16, v249
	v_fmac_f32_e32 v19, v228, v18
	v_and_b32_e32 v18, 0xffff0000, v249
	v_fmac_f32_e32 v19, v229, v18
	v_add_f32_e32 v30, v30, v19
	s_nop 0
	s_nop 0
	s_nop 0
	s_waitcnt lgkmcnt(6)
	v_mfma_f32_32x32x16_bf16 v[2:17], v[230:233], v[210:213], v[2:17]
	s_nop 0
	s_nop 0
	v_lshlrev_b32_e32 v31, 16, v210
	v_and_b32_e32 v22, 0xffff0000, v210
	s_nop 0
	s_waitcnt lgkmcnt(5)
	v_mul_f32_e32 v19, v223, v22
	v_fmac_f32_e32 v19, v222, v31
	v_lshlrev_b32_e32 v18, 16, v211
	v_fmac_f32_e32 v19, v224, v18
	v_and_b32_e32 v18, 0xffff0000, v211
	v_fmac_f32_e32 v19, v225, v18
	v_lshlrev_b32_e32 v18, 16, v212
	s_nop 0
	s_waitcnt lgkmcnt(4)
	v_fmac_f32_e32 v19, v234, v18
	v_and_b32_e32 v18, 0xffff0000, v212
	v_fmac_f32_e32 v19, v235, v18
	v_lshlrev_b32_e32 v18, 16, v213
	v_fmac_f32_e32 v19, v236, v18
	v_and_b32_e32 v18, 0xffff0000, v213
	v_fmac_f32_e32 v19, v237, v18
	v_add_f32_e32 v30, v30, v19
	s_nop 0
	s_nop 0
	s_nop 0
	s_waitcnt lgkmcnt(2)
	v_mfma_f32_32x32x16_bf16 v[2:17], v[238:241], v[214:217], v[2:17]
	s_nop 0
	s_nop 0
	v_lshlrev_b32_e32 v31, 16, v214
	v_and_b32_e32 v22, 0xffff0000, v214
	s_nop 0
	s_waitcnt lgkmcnt(1)
	v_mul_f32_e32 v19, v243, v22
	v_fmac_f32_e32 v19, v242, v31
	v_lshlrev_b32_e32 v18, 16, v215
	v_fmac_f32_e32 v19, v244, v18
	v_and_b32_e32 v18, 0xffff0000, v215
	v_fmac_f32_e32 v19, v245, v18
	v_lshlrev_b32_e32 v18, 16, v216
	s_nop 0
	s_waitcnt lgkmcnt(0)
	v_fmac_f32_e32 v19, v250, v18
	v_and_b32_e32 v18, 0xffff0000, v216
	v_fmac_f32_e32 v19, v251, v18
	v_lshlrev_b32_e32 v18, 16, v217
	v_fmac_f32_e32 v19, v252, v18
	v_and_b32_e32 v18, 0xffff0000, v217
	v_fmac_f32_e32 v19, v253, v18
	v_add_f32_e32 v18, v30, v19
	ds_bpermute_b32 v19, v119, v18
	s_waitcnt lgkmcnt(0)
	v_add_f32_e32 v18, v18, v19
	v_max_f32_e32 v19, v179, v179
	v_max_f32_e64 v18, |v18|, v19
	v_div_scale_f32 v19, s[46:47], v18, v18, 1.0
	v_rcp_f32_e32 v20, v19
	s_nop 0
	v_fma_f32 v21, -v19, v20, 1.0
	v_fmac_f32_e32 v20, v21, v20
	v_div_scale_f32 v21, vcc, 1.0, v18, 1.0
	v_mul_f32_e32 v22, v21, v20
	v_fma_f32 v23, -v19, v22, v21
	v_fmac_f32_e32 v22, v23, v20
	v_fma_f32 v19, -v19, v22, v21
	v_div_fmas_f32 v19, v19, v20, v22
	v_div_fixup_f32 v27, v19, v18, 1.0
	v_mul_f32_e32 v25, v3, v27
	v_mul_f32_e32 v26, v2, v27
	v_mul_f32_e32 v2, v25, v25
	v_fmac_f32_e32 v2, v26, v26
	v_mul_f32_e32 v24, v4, v27
	v_fmac_f32_e32 v2, v24, v24
	v_mul_f32_e32 v23, v5, v27
	v_fmac_f32_e32 v2, v23, v23
	v_mul_f32_e32 v22, v6, v27
	v_fmac_f32_e32 v2, v22, v22
	v_mul_f32_e32 v21, v7, v27
	v_fmac_f32_e32 v2, v21, v21
	v_mul_f32_e32 v20, v8, v27
	v_fmac_f32_e32 v2, v20, v20
	v_mul_f32_e32 v19, v9, v27
	v_fmac_f32_e32 v2, v19, v19
	v_mul_f32_e32 v18, v10, v27
	v_fmac_f32_e32 v2, v18, v18
	v_mul_f32_e32 v11, v11, v27
	v_fmac_f32_e32 v2, v11, v11
	v_mul_f32_e32 v10, v12, v27
	v_fmac_f32_e32 v2, v10, v10
	v_mul_f32_e32 v9, v13, v27
	v_fmac_f32_e32 v2, v9, v9
	v_mul_f32_e32 v7, v14, v27
	v_fmac_f32_e32 v2, v7, v7
	v_mul_f32_e32 v6, v15, v27
	v_fmac_f32_e32 v2, v6, v6
	v_mul_f32_e32 v5, v16, v27
	v_fmac_f32_e32 v2, v5, v5
	v_mul_f32_e32 v4, v17, v27
	v_fmac_f32_e32 v2, v4, v4
	ds_bpermute_b32 v3, v119, v2
	s_and_saveexec_b64 s[46:47], s[44:45]
	s_cbranch_execz .LBB0_1786
	s_waitcnt lgkmcnt(0)
	v_add_f32_e32 v2, v2, v3
	v_add_u32_e32 v3, s4, v148
	ds_write_b32 v3, v2
	s_branch .LBB0_1786
